# v7 + P7 epilogue: one touch load per later residual group right after the first group's loads (lines arrive in L2 before their group)
# baseline (speedup 1.0000x reference)
.LBB0_925:
	v_lshl_add_u32 v150, s28, 8, v1
	v_lshl_or_b32 v146, s4, 8, v224
	v_ashrrev_i32_e32 v147, 31, v146
	v_ashrrev_i32_e32 v151, 31, v150
	v_lshl_add_u64 v[148:149], v[146:147], 2, s[2:3]
	v_lshlrev_b64 v[130:131], 13, v[150:151]
	v_lshl_add_u64 v[130:131], v[148:149], 0, v[130:131]
	global_load_dwordx4 v[156:159], v[130:131], off
	global_load_dwordx4 v[160:163], v[130:131], off offset:16
	global_load_dwordx4 v[164:167], v[130:131], off offset:512
	global_load_dwordx4 v[168:171], v[130:131], off offset:528
	v_or_b32_e32 v152, 16, v150
	v_ashrrev_i32_e32 v153, 31, v152
	v_lshlrev_b64 v[130:131], 13, v[152:153]
	v_lshl_add_u64 v[134:135], v[148:149], 0, v[130:131]
	global_load_dwordx4 v[138:141], v[134:135], off offset:16
	global_load_dwordx4 v[142:145], v[134:135], off
	global_load_dwordx4 v[130:133], v[134:135], off offset:528
	s_nop 0
	global_load_dwordx4 v[134:137], v[134:135], off offset:512
	v_lshlrev_b64 v[176:177], 13, v[150:151]
	v_lshrrev_b32_e32 v178, 4, v228
	v_lshl_add_u64 v[176:177], v[148:149], 0, v[176:177]
	v_and_b32_e32 v179, 1, v178
	v_lshrrev_b32_e32 v180, 1, v178
	v_lshlrev_b32_e32 v179, 17, v179
	v_lshlrev_b32_e32 v178, 5, v178
	v_lshl_add_u32 v180, v180, 9, v179
	v_mov_b32_e32 v181, 0
	v_sub_u32_e32 v180, v180, v178
	v_mov_b32_e32 v188, 0x40000
	v_mov_b32_e32 v189, 0
	v_lshl_add_u64 v[176:177], v[176:177], 0, v[180:181]
	v_lshl_add_u64 v[182:183], v[176:177], 0, v[188:189]
	v_lshl_add_u64 v[184:185], v[188:189], 2, v[176:177]
	global_load_dword v190, v[182:183], off
	v_lshl_add_u64 v[186:187], v[188:189], 0, v[184:185]
	global_load_dword v191, v[184:185], off
	global_load_dword v192, v[186:187], off
	v_and_b32_e32 v154, 64, v228
	v_xor_b32_e32 v172, 16, v228
	v_add_u32_e32 v174, 64, v154
	v_xor_b32_e32 v173, 32, v228
	v_cmp_lt_i32_e32 vcc, v172, v174
	v_lshlrev_b64 v[154:155], 12, v[150:151]
	s_lshl_b32 s28, s4, 2
	v_cndmask_b32_e32 v175, v228, v172, vcc
	v_cmp_lt_i32_e32 vcc, v173, v174
	s_ashr_i32 s29, s28, 31
	s_waitcnt vmcnt(0)
	v_pk_add_f32 v[128:129], v[128:129], v[158:159]
	v_pk_add_f32 v[126:127], v[126:127], v[156:157]
	v_pk_add_f32 v[124:125], v[124:125], v[162:163]
	v_pk_add_f32 v[122:123], v[122:123], v[160:161]
	v_pk_add_f32 v[156:157], v[120:121], v[166:167]
	v_pk_add_f32 v[118:119], v[118:119], v[164:165]
	v_pk_add_f32 v[158:159], v[116:117], v[170:171]
	v_pk_add_f32 v[160:161], v[114:115], v[168:169]
	v_cndmask_b32_e32 v174, v228, v173, vcc
	v_lshl_add_u64 v[172:173], s[12:13], 0, v[154:155]
	v_cvt_pk_bf16_f32 v114, v126, v127
	v_cvt_pk_bf16_f32 v115, v128, v129
	v_mul_f32_e32 v116, v127, v127
	v_mul_f32_e32 v117, v129, v129
	v_mul_f32_e32 v120, v123, v123
	v_mul_f32_e32 v121, v125, v125
	v_mul_f32_e32 v127, v119, v119
	v_mul_f32_e32 v129, v157, v157
	v_mul_f32_e32 v155, v161, v161
	v_mul_f32_e32 v162, v159, v159
	v_fmac_f32_e32 v116, v126, v126
	v_fmac_f32_e32 v117, v128, v128
	v_fmac_f32_e32 v120, v122, v122
	v_fmac_f32_e32 v121, v124, v124
	v_fmac_f32_e32 v127, v118, v118
	v_fmac_f32_e32 v129, v156, v156
	v_fmac_f32_e32 v155, v160, v160
	v_fmac_f32_e32 v162, v158, v158
	v_add_f32_e32 v116, v116, v117
	v_add_f32_e32 v117, v120, v121
	v_add_f32_e32 v120, v127, v129
	v_add_f32_e32 v121, v155, v162
	v_add_f32_e32 v116, v116, v117
	v_add_f32_e32 v117, v120, v121
	v_lshlrev_b32_e32 v154, 2, v175
	v_add_f32_e32 v121, v116, v117
	ds_bpermute_b32 v126, v154, v121
	v_lshl_add_u64 v[172:173], v[146:147], 1, v[172:173]
	v_cvt_pk_bf16_f32 v116, v122, v123
	v_cvt_pk_bf16_f32 v117, v124, v125
	global_store_dwordx4 v[172:173], v[114:117], off
	v_cvt_pk_bf16_f32 v120, v118, v119
	v_lshlrev_b32_e32 v118, 2, v174
	s_waitcnt lgkmcnt(0)
	v_add_f32_e32 v114, v121, v126
	ds_bpermute_b32 v115, v118, v114
	v_cvt_pk_bf16_f32 v121, v156, v157
	v_cvt_pk_bf16_f32 v122, v160, v161
	v_cvt_pk_bf16_f32 v123, v158, v159
	global_store_dwordx4 v[172:173], v[120:123], off offset:256
	s_and_saveexec_b64 s[30:31], s[8:9]
	s_cbranch_execz .LBB0_927
	v_lshlrev_b64 v[116:117], 7, v[150:151]
	v_lshl_add_u64 v[116:117], s[14:15], 0, v[116:117]
	v_lshl_add_u64 v[116:117], s[28:29], 2, v[116:117]
	s_lshl_b32 s4, s58, 2
	v_lshl_add_u64 v[116:117], v[116:117], 0, s[4:5]
	s_waitcnt lgkmcnt(0)
	v_add_f32_e32 v114, v114, v115
	global_store_dword v[116:117], v114, off
